# combination: attention decode ballot trim + store-aware first-unit wait in G1 + retention-gate epilogue load prefetch, on top of the rotated K-loops
# baseline (speedup 1.0000x reference)
; #define PG8_WAIT_V(n) asm volatile("s_waitcnt vmcnt(" #n ")" ::: "memory")
; #define PG8_BAR __builtin_amdgcn_s_barrier()
; template <class Epi, class Sched, bool ALIGN_EPI = false, bool SP2 = false>
; __device__ __forceinline__ void gemm_phase(PG8_LAS unsigned char* lds, const Gemm g, const Sched& S, const Epi& E, const int tid) {
;     const int wid = __builtin_amdgcn_readfirstlane(tid >> 6), lane = tid & 63, wr = wid >> 2, wc = wid & 3, fr = lane & 15, fq = lane >> 4;
;     const int K = g.K, nt = K / BK;
;     unsigned voffA[2], voffB[2], voffB1[2];
; #pragma unroll
;     for (int i = 0; i < 2; ++i) { int R, C; stage_rc(tid * 16 + i * 8192, R, C); const int Rb = Epi::PERM ? ((R & ~31) + perm32(R & 31)) : R;
;         voffA[i] = (unsigned)(R * K + C) * 2u; { const int ld = g.ldil, lper = 8 - ld, pm1 = (1 << lper) - 1; const int c0 = Rb, c1 = 128 + Rb; voffB[i] = (unsigned)((((c0 & pm1) << ld) + (c0 >> lper)) * K + C) * 2u; voffB1[i] = (unsigned)((((c1 & pm1) << ld) + (c1 >> lper)) * K + C) * 2u; } }
;     const size_t kstep = (size_t)(BK * 2);
;     const size_t hstep = (size_t)HALF * K * 2;
;     const size_t tstep = 2 * hstep;
;     const unsigned ldsw = (unsigned)wid * 1024u;
;     const int aoff = lds_byte(wr * 64 + fr, fq * 8), boff = lds_byte(wc * 32 + fr, fq * 8);
;     ...
;     Unit cur, nxt; int ui = 0;
;     if (!S.next(0, cur)) return;
;     f32x4 acc[2][2][4][2];
; #pragma unroll
;     for (int a = 0; a < 2; ++a)
; #pragma unroll
;         for (int b = 0; b < 2; ++b)
; #pragma unroll
;             for (int m = 0; m < 4; ++m)
; #pragma unroll
;                 for (int n = 0; n < 2; ++n) acc[a][b][m][n] = (f32x4){0.f, 0.f, 0.f, 0.f};
;     bf16x8 At[4][2], B0[2][2], B1[2][2];
;     const char* cA = (const char*)g.A + (size_t)cur.pm * tstep; const char* cB = (const char*)g.Bt + (size_t)cur.pn * tstep;
;     S.a_ready(cur);
;     if constexpr (SP2) {
;         PG8_STAGE(PG8_SB(0, 0), cB, voffB); PG8_STAGE(PG8_SB(0, 1), cB, voffB1); PG8_STAGE(PG8_SA(0, 0), cA, voffA); PG8_STAGE(PG8_SA(0, 1), cA + hstep, voffA);
;         if (wr == 1) PG8_BAR;
;         PG8_WAIT_V(2); PG8_BAR;
;         PG8_STAGE(PG8_SB(1, 0), cB + kstep, voffB); PG8_STAGE(PG8_SA(1, 0), cA + kstep, voffA); PG8_STAGE(PG8_SB(1, 1), cB + kstep, voffB1);
;         PG8_WAIT_V(6); PG8_BAR;
.LBB0_721:
	s_add_u32 s4, s96, 0xda00000
	s_addc_u32 s5, s97, 0
	s_add_i32 m0, s43, 0x18000
	v_lshl_add_u64 v[10:11], v[10:11], 0, s[66:67]
	s_waitcnt vmcnt(2)
	s_barrier
	global_load_lds_dwordx4 v[10:11], off
	v_lshl_add_u64 v[8:9], v[8:9], 0, s[66:67]
	s_add_i32 m0, s43, 0x1a000
	s_add_i32 s50, s43, 0x8000
	global_load_lds_dwordx4 v[8:9], off
	v_lshl_add_u64 v[8:9], v[12:13], 0, s[66:67]
	s_mov_b32 m0, s50
	s_add_i32 s51, s43, 0xa000
	global_load_lds_dwordx4 v[8:9], off
	v_lshl_add_u64 v[8:9], v[14:15], 0, s[66:67]
	s_mov_b32 m0, s51
	v_lshl_add_u64 v[6:7], v[6:7], 0, s[66:67]
	global_load_lds_dwordx4 v[8:9], off
	s_add_i32 m0, s43, 0x1c000
	v_lshl_add_u64 v[4:5], v[4:5], 0, s[66:67]
	global_load_lds_dwordx4 v[6:7], off
	s_add_i32 m0, s43, 0x1e000
	s_sext_i32_i16 s57, s2
	global_load_lds_dwordx4 v[4:5], off
	v_lshrrev_b32_e32 v5, 1, v16
	v_and_b32_e32 v5, 24, v5
	v_and_b32_e32 v4, 15, v16
	s_lshl_b32 s2, s7, 6
	v_lshlrev_b32_e32 v6, 1, v5
	v_or_b32_e32 v150, s2, v4
	v_lshl_or_b32 v6, v4, 6, v6
	s_lshl_b32 s6, s6, 5
	v_bitop3_b32 v152, s2, v240, v4 bitop3:0xc8
	v_lshlrev_b32_e32 v4, 14, v21
	s_and_b32 s8, s6, 0x60
	v_and_b32_e32 v4, 0xffff8000, v4
	v_or_b32_e32 v153, s8, v5
	v_lshl_add_u32 v4, v20, 11, v4
	v_and_b32_e32 v5, 1, v21
	v_lshl_or_b32 v4, v5, 6, v4
	v_lshl_add_u32 v140, v22, 1, v4
	v_lshlrev_b32_e32 v4, 14, v17
	v_lshlrev_b32_e32 v7, 2, v16
	v_and_b32_e32 v4, 0xffff8000, v4
	s_lshl_b32 s7, s7, 13
	v_and_b32_e32 v7, 32, v7
	s_lshl_b32 s6, s8, 7
	s_waitcnt vmcnt(6)
	v_lshl_add_u32 v4, v18, 11, v4
	v_and_b32_e32 v5, 1, v17
	v_bitop3_b32 v8, v6, s7, v7 bitop3:0xde
	s_cmpk_lt_u32 s3, 0x100
	v_lshl_or_b32 v4, v5, 6, v4
	v_bitop3_b32 v151, s6, v6, v7 bitop3:0xf6
	s_cselect_b64 s[6:7], -1, 0
	s_ashr_i32 s54, s88, 31
	v_mov_b32_e32 v141, v3
	v_lshl_add_u32 v142, v19, 1, v4
	v_mov_b32_e32 v143, v3
	s_mov_b32 s58, 0
	v_add_u32_e32 v154, 0, v8
	s_mov_b32 s55, 0
	s_barrier
	s_mov_b32 s32, 0
	s_branch .LBB0_724

; #define PG8_STAGE(bufoff, gbase, voff) do { _Pragma("unroll") for (int _i = 0; _i < 2; ++_i) \
;         __builtin_amdgcn_global_load_lds((const unsigned*)((const char*)(gbase) + (voff)[_i]), (PG8_LAS unsigned*)(lds + (bufoff) + ldsw + _i * 8192), 16, 0, 0); } while (0)
; #define PG8_LDA(dst, b, h) do { _Pragma("unroll") for (int m = 0; m < 4; ++m) _Pragma("unroll") for (int k = 0; k < 2; ++k) dst[m][k] = *(const PG8_LAS bf16x8*)(lds + PG8_SA(b, h) + aoff + m * 2048 + k * 1024); } while (0)
; #define PG8_LDB(dst, b, h) do { _Pragma("unroll") for (int n = 0; n < 2; ++n) _Pragma("unroll") for (int k = 0; k < 2; ++k) dst[n][k] = *(const PG8_LAS bf16x8*)(lds + PG8_SB(b, h) + boff + n * 2048 + k * 1024); } while (0)
; #define PG8_MMA(ai, bj, At, Bt) do { __builtin_amdgcn_s_setprio(1); _Pragma("unroll") for (int m = 0; m < 4; ++m) _Pragma("unroll") for (int n = 0; n < 2; ++n) _Pragma("unroll") for (int k = 0; k < 2; ++k) \
;         acc[ai][bj][m][n] = __builtin_amdgcn_mfma_f32_16x16x32_bf16(Bt[n][k], At[m][k], acc[ai][bj][m][n], 0, 0, 0); __builtin_amdgcn_s_setprio(0); } while (0)
; #define PG8_WAIT_V(n) asm volatile("s_waitcnt vmcnt(" #n ")" ::: "memory")
; #define PG8_BAR __builtin_amdgcn_s_barrier()
; template <class Epi, class Sched, bool ALIGN_EPI = false, bool SP2 = false>
; __device__ __forceinline__ void gemm_phase(PG8_LAS unsigned char* lds, const Gemm g, const Sched& S, const Epi& E, const int tid) {
;     ...
;         for (int t = 0; t < nt; t += 2) {
;             const bool last = (t == nt - 2);
;             const char* a1 = cA + (size_t)(t + 1) * kstep;
;             const char* a2 = last ? nA : cA + (size_t)(t + 2) * kstep; const char* b2 = last ? nB : cB + (size_t)(t + 2) * kstep;
;             const char* a3 = a2 + kstep; const char* b3 = b2 + kstep;
;             if (last && has_next) S.a_ready(nxt);
;             if constexpr (SP2) {
;             PG8_LDB(B0, 0, 0); PG8_LDB(B1, 0, 1); PG8_SCHED; PG8_LDA(At, 0, 0); PG8_STAGE(PG8_SA(1, 1), a1 + hstep, voffA);
;             PG8_WAIT_V(8); PG8_WAIT_L(0); PG8_BAR; PG8_MMA(0, 0, At, B0); PG8_MMA(0, 1, At, B1); PG8_BAR; PG8_SCHED;
;             PG8_LDA(At, 0, 1); PG8_STAGE(PG8_SB(0, 0), b2, voffB); PG8_STAGE(PG8_SB(0, 1), b2, voffB1); PG8_STAGE(PG8_SA(0, 0), a2, voffA);
;             PG8_WAIT_V(8); PG8_WAIT_L(0); PG8_BAR; PG8_MMA(1, 0, At, B0); PG8_MMA(1, 1, At, B1); PG8_BAR; PG8_SCHED;
.LBB0_724:
.LBB0_726:
	s_add_u32 s46, s46, 0x40080
	s_addc_u32 s47, s47, 0
	s_add_u32 s52, s52, 0x100
	s_addc_u32 s53, s53, 0
	s_mov_b32 s62, -2
	s_add_u32 s36, s46, 0xfffc0080
	s_addc_u32 s37, s47, -1
	s_add_i32 s63, 0, 0x10000
	s_cmp_eq_u32 s62, 12
	s_cselect_b32 s37, s11, s37
	s_cselect_b32 s36, s59, s36
	v_add_u32_e32 v148, s63, v151
	s_cselect_b32 s73, s9, s53
	s_cselect_b32 s72, s60, s52
	s_add_i32 s68, 0, 0x14000
	ds_read_b128 v[144:147], v148
	ds_read_b128 v[156:159], v148 offset:1024
	ds_read_b128 v[160:163], v148 offset:2048
	ds_read_b128 v[164:167], v148 offset:3072
	v_add_u32_e32 v148, s68, v151
	ds_read_b128 v[168:171], v148
	ds_read_b128 v[172:175], v148 offset:1024
	ds_read_b128 v[176:179], v148 offset:2048
	ds_read_b128 v[180:183], v148 offset:3072
	v_lshl_add_u64 v[148:149], s[46:47], 0, v[140:141]
	s_add_i32 m0, s43, 0xc000
	ds_read_b128 v[184:187], v154
	ds_read_b128 v[188:191], v154 offset:1024
	ds_read_b128 v[192:195], v154 offset:2048
	ds_read_b128 v[196:199], v154 offset:3072
	ds_read_b128 v[212:215], v154 offset:4096
	ds_read_b128 v[216:219], v154 offset:5120
	ds_read_b128 v[220:223], v154 offset:6144
	ds_read_b128 v[224:227], v154 offset:7168
	global_load_lds_dwordx4 v[148:149], off
	v_lshl_add_u64 v[148:149], s[46:47], 0, v[142:143]
	s_add_i32 m0, s43, 0xe000
	s_nop 0
	global_load_lds_dwordx4 v[148:149], off
	s_waitcnt vmcnt(8)
	s_waitcnt lgkmcnt(0)
	s_barrier
	s_setprio 1
	s_waitcnt lgkmcnt(0)
	v_mfma_f32_16x16x32_bf16 v[128:131], v[144:147], v[184:187], 0
	v_mfma_f32_16x16x32_bf16 v[120:123], v[160:163], v[184:187], 0
	v_mfma_f32_16x16x32_bf16 v[112:115], v[144:147], v[192:195], 0
	v_mfma_f32_16x16x32_bf16 v[104:107], v[160:163], v[192:195], 0
	v_mfma_f32_16x16x32_bf16 v[96:99], v[144:147], v[212:215], 0
	v_mfma_f32_16x16x32_bf16 v[88:91], v[160:163], v[212:215], 0
	v_mfma_f32_16x16x32_bf16 v[80:83], v[144:147], v[220:223], 0
	v_mfma_f32_16x16x32_bf16 v[72:75], v[160:163], v[220:223], 0
	v_mfma_f32_16x16x32_bf16 v[128:131], v[156:159], v[188:191], v[128:131]
	v_mfma_f32_16x16x32_bf16 v[120:123], v[164:167], v[188:191], v[120:123]
	v_mfma_f32_16x16x32_bf16 v[112:115], v[156:159], v[196:199], v[112:115]
	v_mfma_f32_16x16x32_bf16 v[104:107], v[164:167], v[196:199], v[104:107]
	v_mfma_f32_16x16x32_bf16 v[96:99], v[156:159], v[216:219], v[96:99]
	v_mfma_f32_16x16x32_bf16 v[88:91], v[164:167], v[216:219], v[88:91]
	v_mfma_f32_16x16x32_bf16 v[80:83], v[156:159], v[224:227], v[80:83]
	v_mfma_f32_16x16x32_bf16 v[72:75], v[164:167], v[224:227], v[72:75]
	s_setprio 0
	s_setprio 1
	v_mfma_f32_16x16x32_bf16 v[124:127], v[168:171], v[184:187], 0
	v_mfma_f32_16x16x32_bf16 v[116:119], v[176:179], v[184:187], 0
	v_mfma_f32_16x16x32_bf16 v[108:111], v[168:171], v[192:195], 0
	v_mfma_f32_16x16x32_bf16 v[100:103], v[176:179], v[192:195], 0
	v_mfma_f32_16x16x32_bf16 v[92:95], v[168:171], v[212:215], 0
	v_mfma_f32_16x16x32_bf16 v[84:87], v[176:179], v[212:215], 0
	v_mfma_f32_16x16x32_bf16 v[76:79], v[168:171], v[220:223], 0
	v_mfma_f32_16x16x32_bf16 v[68:71], v[176:179], v[220:223], 0
	v_mfma_f32_16x16x32_bf16 v[124:127], v[172:175], v[188:191], v[124:127]
	v_mfma_f32_16x16x32_bf16 v[116:119], v[180:183], v[188:191], v[116:119]
	v_mfma_f32_16x16x32_bf16 v[108:111], v[172:175], v[196:199], v[108:111]
	v_mfma_f32_16x16x32_bf16 v[100:103], v[180:183], v[196:199], v[100:103]
	v_mfma_f32_16x16x32_bf16 v[92:95], v[172:175], v[216:219], v[92:95]
	v_mfma_f32_16x16x32_bf16 v[84:87], v[180:183], v[216:219], v[84:87]
	v_mfma_f32_16x16x32_bf16 v[76:79], v[172:175], v[224:227], v[76:79]
	v_mfma_f32_16x16x32_bf16 v[68:71], v[180:183], v[224:227], v[68:71]
	s_setprio 0
	s_barrier
	s_add_i32 s63, s63, s33
	v_lshl_add_u64 v[148:149], s[72:73], 0, v[2:3]
	s_mov_b32 m0, s63
	ds_read_b128 v[184:187], v154 offset:16384
	ds_read_b128 v[188:191], v154 offset:17408
	ds_read_b128 v[192:195], v154 offset:18432
	ds_read_b128 v[196:199], v154 offset:19456
	ds_read_b128 v[212:215], v154 offset:20480
	ds_read_b128 v[216:219], v154 offset:21504
	ds_read_b128 v[220:223], v154 offset:22528
	ds_read_b128 v[224:227], v154 offset:23552
	global_load_lds_dwordx4 v[148:149], off
	v_lshl_add_u64 v[200:201], s[72:73], 0, v[132:133]
	s_add_i32 m0, s63, 0x2000
	s_add_i32 s63, s68, s33
	global_load_lds_dwordx4 v[200:201], off
	v_lshl_add_u64 v[202:203], s[72:73], 0, v[136:137]
	s_mov_b32 m0, s63
	v_lshl_add_u64 v[204:205], s[72:73], 0, v[0:1]
	global_load_lds_dwordx4 v[202:203], off
	s_add_i32 m0, s63, 0x2000
	v_lshl_add_u64 v[208:209], s[36:37], 0, v[138:139]
	global_load_lds_dwordx4 v[204:205], off
	s_mov_b32 m0, s43
	v_lshl_add_u64 v[210:211], s[36:37], 0, v[134:135]
	global_load_lds_dwordx4 v[208:209], off
	s_mov_b32 m0, s45
	s_nop 0
	global_load_lds_dwordx4 v[210:211], off
	s_cmp_eq_u32 s32, 0
	s_cbranch_scc1 .Lg1_w8
	s_waitcnt vmcnt(16)
	s_branch .Lg1_wd
.Lg1_w8:
	s_waitcnt vmcnt(8)
; #define PG8_STAGE(bufoff, gbase, voff) do { _Pragma("unroll") for (int _i = 0; _i < 2; ++_i) \
;         __builtin_amdgcn_global_load_lds((const unsigned*)((const char*)(gbase) + (voff)[_i]), (PG8_LAS unsigned*)(lds + (bufoff) + ldsw + _i * 8192), 16, 0, 0); } while (0)
; #define PG8_LDA(dst, b, h) do { _Pragma("unroll") for (int m = 0; m < 4; ++m) _Pragma("unroll") for (int k = 0; k < 2; ++k) dst[m][k] = *(const PG8_LAS bf16x8*)(lds + PG8_SA(b, h) + aoff + m * 2048 + k * 1024); } while (0)
; #define PG8_LDB(dst, b, h) do { _Pragma("unroll") for (int n = 0; n < 2; ++n) _Pragma("unroll") for (int k = 0; k < 2; ++k) dst[n][k] = *(const PG8_LAS bf16x8*)(lds + PG8_SB(b, h) + boff + n * 2048 + k * 1024); } while (0)
; #define PG8_MMA(ai, bj, At, Bt) do { __builtin_amdgcn_s_setprio(1); _Pragma("unroll") for (int m = 0; m < 4; ++m) _Pragma("unroll") for (int n = 0; n < 2; ++n) _Pragma("unroll") for (int k = 0; k < 2; ++k) \
;         acc[ai][bj][m][n] = __builtin_amdgcn_mfma_f32_16x16x32_bf16(Bt[n][k], At[m][k], acc[ai][bj][m][n], 0, 0, 0); __builtin_amdgcn_s_setprio(0); } while (0)
; #define PG8_WAIT_V(n) asm volatile("s_waitcnt vmcnt(" #n ")" ::: "memory")
; #define PG8_WAIT_L(n) asm volatile("s_waitcnt lgkmcnt(" #n ")" ::: "memory")
; #define PG8_BAR __builtin_amdgcn_s_barrier()
; #define PG8_SCHED __builtin_amdgcn_sched_barrier(0)
; template <class Epi, class Sched, bool ALIGN_EPI = false, bool SP2 = false>
; __device__ __forceinline__ void gemm_phase(PG8_LAS unsigned char* lds, const Gemm g, const Sched& S, const Epi& E, const int tid) {
;     ...
;             PG8_WAIT_V(8); PG8_WAIT_L(0); PG8_BAR; PG8_MMA(1, 0, At, B0); PG8_MMA(1, 1, At, B1); PG8_BAR; PG8_SCHED;
;             PG8_LDB(B0, 1, 0); PG8_LDB(B1, 1, 1); PG8_SCHED; PG8_LDA(At, 1, 0); PG8_STAGE(PG8_SA(0, 1), a2 + hstep, voffA);
;             PG8_WAIT_V(8); PG8_WAIT_L(0); PG8_BAR; PG8_MMA(0, 0, At, B0); PG8_MMA(0, 1, At, B1); PG8_BAR; PG8_SCHED;
.Lg1_wd:
	s_waitcnt lgkmcnt(0)
	s_barrier
	s_setprio 1
	s_waitcnt lgkmcnt(0)
	v_mfma_f32_16x16x32_bf16 v[64:67], v[144:147], v[184:187], 0
	v_mfma_f32_16x16x32_bf16 v[56:59], v[160:163], v[184:187], 0
	v_mfma_f32_16x16x32_bf16 v[48:51], v[144:147], v[192:195], 0
	v_mfma_f32_16x16x32_bf16 v[40:43], v[160:163], v[192:195], 0
	v_mfma_f32_16x16x32_bf16 v[32:35], v[144:147], v[212:215], 0
	v_mfma_f32_16x16x32_bf16 v[24:27], v[160:163], v[212:215], 0
	v_mfma_f32_16x16x32_bf16 v[16:19], v[144:147], v[220:223], 0
	v_mfma_f32_16x16x32_bf16 v[8:11], v[160:163], v[220:223], 0
	v_mfma_f32_16x16x32_bf16 v[64:67], v[156:159], v[188:191], v[64:67]
	v_mfma_f32_16x16x32_bf16 v[56:59], v[164:167], v[188:191], v[56:59]
	v_mfma_f32_16x16x32_bf16 v[48:51], v[156:159], v[196:199], v[48:51]
	v_mfma_f32_16x16x32_bf16 v[40:43], v[164:167], v[196:199], v[40:43]
	v_mfma_f32_16x16x32_bf16 v[32:35], v[156:159], v[216:219], v[32:35]
	v_mfma_f32_16x16x32_bf16 v[24:27], v[164:167], v[216:219], v[24:27]
	v_mfma_f32_16x16x32_bf16 v[16:19], v[156:159], v[224:227], v[16:19]
	v_mfma_f32_16x16x32_bf16 v[8:11], v[164:167], v[224:227], v[8:11]
	s_setprio 0
	s_setprio 1
	v_mfma_f32_16x16x32_bf16 v[60:63], v[168:171], v[184:187], 0
	v_mfma_f32_16x16x32_bf16 v[52:55], v[176:179], v[184:187], 0
	v_mfma_f32_16x16x32_bf16 v[44:47], v[168:171], v[192:195], 0
	v_mfma_f32_16x16x32_bf16 v[36:39], v[176:179], v[192:195], 0
	v_mfma_f32_16x16x32_bf16 v[28:31], v[168:171], v[212:215], 0
	v_mfma_f32_16x16x32_bf16 v[20:23], v[176:179], v[212:215], 0
	v_mfma_f32_16x16x32_bf16 v[12:15], v[168:171], v[220:223], 0
	v_mfma_f32_16x16x32_bf16 v[4:7], v[176:179], v[220:223], 0
	v_mfma_f32_16x16x32_bf16 v[60:63], v[172:175], v[188:191], v[60:63]
	v_mfma_f32_16x16x32_bf16 v[52:55], v[180:183], v[188:191], v[52:55]
	v_mfma_f32_16x16x32_bf16 v[44:47], v[172:175], v[196:199], v[44:47]
	v_mfma_f32_16x16x32_bf16 v[36:39], v[180:183], v[196:199], v[36:39]
	v_mfma_f32_16x16x32_bf16 v[28:31], v[172:175], v[216:219], v[28:31]
	v_mfma_f32_16x16x32_bf16 v[20:23], v[180:183], v[216:219], v[20:23]
	v_mfma_f32_16x16x32_bf16 v[12:15], v[172:175], v[224:227], v[12:15]
	v_mfma_f32_16x16x32_bf16 v[4:7], v[180:183], v[224:227], v[4:7]
	s_setprio 0
	s_barrier
	s_add_i32 s63, 0, 0x18000
	v_add_u32_e32 v155, s63, v151
	s_add_i32 s68, 0, 0x1c000
	ds_read_b128 v[144:147], v155
	ds_read_b128 v[156:159], v155 offset:1024
	ds_read_b128 v[160:163], v155 offset:2048
	ds_read_b128 v[164:167], v155 offset:3072
	v_add_u32_e32 v155, s68, v151
	ds_read_b128 v[168:171], v155
	ds_read_b128 v[172:175], v155 offset:1024
	ds_read_b128 v[176:179], v155 offset:2048
	ds_read_b128 v[180:183], v155 offset:3072
	s_add_u32 s36, s36, 0x40000
	s_addc_u32 s37, s37, 0
	s_mov_b32 m0, s48
	v_lshl_add_u64 v[228:229], s[36:37], 0, v[138:139]
	ds_read_b128 v[184:187], v154 offset:32768
	ds_read_b128 v[188:191], v154 offset:33792
	ds_read_b128 v[192:195], v154 offset:34816
	ds_read_b128 v[196:199], v154 offset:35840
	ds_read_b128 v[212:215], v154 offset:36864
	ds_read_b128 v[216:219], v154 offset:37888
	ds_read_b128 v[220:223], v154 offset:38912
	ds_read_b128 v[224:227], v154 offset:39936
	global_load_lds_dwordx4 v[228:229], off
	v_lshl_add_u64 v[228:229], s[36:37], 0, v[134:135]
	s_mov_b32 m0, s49
	s_nop 0
	global_load_lds_dwordx4 v[228:229], off
	s_waitcnt vmcnt(8)
	s_waitcnt lgkmcnt(0)
	s_barrier
	s_setprio 1
	s_waitcnt lgkmcnt(0)
	v_mfma_f32_16x16x32_bf16 v[128:131], v[144:147], v[184:187], v[128:131]
	v_mfma_f32_16x16x32_bf16 v[120:123], v[160:163], v[184:187], v[120:123]
	v_mfma_f32_16x16x32_bf16 v[112:115], v[144:147], v[192:195], v[112:115]
	v_mfma_f32_16x16x32_bf16 v[104:107], v[160:163], v[192:195], v[104:107]
	v_mfma_f32_16x16x32_bf16 v[96:99], v[144:147], v[212:215], v[96:99]
	v_mfma_f32_16x16x32_bf16 v[88:91], v[160:163], v[212:215], v[88:91]
	v_mfma_f32_16x16x32_bf16 v[80:83], v[144:147], v[220:223], v[80:83]
	v_mfma_f32_16x16x32_bf16 v[72:75], v[160:163], v[220:223], v[72:75]
	v_mfma_f32_16x16x32_bf16 v[128:131], v[156:159], v[188:191], v[128:131]
	v_mfma_f32_16x16x32_bf16 v[120:123], v[164:167], v[188:191], v[120:123]
	v_mfma_f32_16x16x32_bf16 v[112:115], v[156:159], v[196:199], v[112:115]
	v_mfma_f32_16x16x32_bf16 v[104:107], v[164:167], v[196:199], v[104:107]
	v_mfma_f32_16x16x32_bf16 v[96:99], v[156:159], v[216:219], v[96:99]
	v_mfma_f32_16x16x32_bf16 v[88:91], v[164:167], v[216:219], v[88:91]
	v_mfma_f32_16x16x32_bf16 v[80:83], v[156:159], v[224:227], v[80:83]
	v_mfma_f32_16x16x32_bf16 v[72:75], v[164:167], v[224:227], v[72:75]
	s_setprio 0
	s_setprio 1
	v_mfma_f32_16x16x32_bf16 v[124:127], v[168:171], v[184:187], v[124:127]
	v_mfma_f32_16x16x32_bf16 v[116:119], v[176:179], v[184:187], v[116:119]
	v_mfma_f32_16x16x32_bf16 v[108:111], v[168:171], v[192:195], v[108:111]
	v_mfma_f32_16x16x32_bf16 v[100:103], v[176:179], v[192:195], v[100:103]
	v_mfma_f32_16x16x32_bf16 v[92:95], v[168:171], v[212:215], v[92:95]
	v_mfma_f32_16x16x32_bf16 v[84:87], v[176:179], v[212:215], v[84:87]
	v_mfma_f32_16x16x32_bf16 v[76:79], v[168:171], v[220:223], v[76:79]
	v_mfma_f32_16x16x32_bf16 v[68:71], v[176:179], v[220:223], v[68:71]
	v_mfma_f32_16x16x32_bf16 v[124:127], v[172:175], v[188:191], v[124:127]
	v_mfma_f32_16x16x32_bf16 v[116:119], v[180:183], v[188:191], v[116:119]
	v_mfma_f32_16x16x32_bf16 v[108:111], v[172:175], v[196:199], v[108:111]
	v_mfma_f32_16x16x32_bf16 v[100:103], v[180:183], v[196:199], v[100:103]
	v_mfma_f32_16x16x32_bf16 v[92:95], v[172:175], v[216:219], v[92:95]
	v_mfma_f32_16x16x32_bf16 v[84:87], v[180:183], v[216:219], v[84:87]
	v_mfma_f32_16x16x32_bf16 v[76:79], v[172:175], v[224:227], v[76:79]
	v_mfma_f32_16x16x32_bf16 v[68:71], v[180:183], v[224:227], v[68:71]
	s_setprio 0
	s_barrier
; #define PG8_STAGE(bufoff, gbase, voff) do { _Pragma("unroll") for (int _i = 0; _i < 2; ++_i) \
;         __builtin_amdgcn_global_load_lds((const unsigned*)((const char*)(gbase) + (voff)[_i]), (PG8_LAS unsigned*)(lds + (bufoff) + ldsw + _i * 8192), 16, 0, 0); } while (0)
; #define PG8_LDA(dst, b, h) do { _Pragma("unroll") for (int m = 0; m < 4; ++m) _Pragma("unroll") for (int k = 0; k < 2; ++k) dst[m][k] = *(const PG8_LAS bf16x8*)(lds + PG8_SA(b, h) + aoff + m * 2048 + k * 1024); } while (0)
; #define PG8_MMA(ai, bj, At, Bt) do { __builtin_amdgcn_s_setprio(1); _Pragma("unroll") for (int m = 0; m < 4; ++m) _Pragma("unroll") for (int n = 0; n < 2; ++n) _Pragma("unroll") for (int k = 0; k < 2; ++k) \
;         acc[ai][bj][m][n] = __builtin_amdgcn_mfma_f32_16x16x32_bf16(Bt[n][k], At[m][k], acc[ai][bj][m][n], 0, 0, 0); __builtin_amdgcn_s_setprio(0); } while (0)
; #define PG8_WAIT_V(n) asm volatile("s_waitcnt vmcnt(" #n ")" ::: "memory")
; #define PG8_WAIT_L(n) asm volatile("s_waitcnt lgkmcnt(" #n ")" ::: "memory")
; #define PG8_BAR __builtin_amdgcn_s_barrier()
; #define PG8_SCHED __builtin_amdgcn_sched_barrier(0)
;     __host__ __device__ bool next(int i, Unit& u) const {
;         const long L = (long)i * G + c; if (L >= nwg) return false;
;         int wgid = (int)L; { const int q = nwg / NXCD, r = nwg % NXCD, xcd = wgid % NXCD, off = wgid / NXCD; wgid = (xcd < r ? xcd * (q + 1) : r * (q + 1) + (xcd - r) * q) + off; }
;         const int nig = WGM * nN, gid = wgid / nig, fm = gid * WGM, gsz = (nM - fm) < WGM ? (nM - fm) : WGM;
;         u.pm = fm + ((wgid % nig) % gsz); u.pn = (wgid % nig) / gsz; u.idx = i; return true;
; template <class Epi, class Sched, bool ALIGN_EPI = false, bool SP2 = false>
; __device__ __forceinline__ void gemm_phase(PG8_LAS unsigned char* lds, const Gemm g, const Sched& S, const Epi& E, const int tid) {
;     ...
;             PG8_WAIT_V(8); PG8_WAIT_L(0); PG8_BAR; PG8_MMA(0, 0, At, B0); PG8_MMA(0, 1, At, B1); PG8_BAR; PG8_SCHED;
;             PG8_LDA(At, 1, 1); PG8_STAGE(PG8_SB(1, 0), b3, voffB); PG8_STAGE(PG8_SB(1, 1), b3, voffB1); PG8_STAGE(PG8_SA(1, 0), a3, voffA);
;             PG8_WAIT_V(8); PG8_WAIT_L(0); PG8_BAR; PG8_MMA(1, 0, At, B0); PG8_MMA(1, 1, At, B1); PG8_BAR; PG8_SCHED;
	s_add_i32 s36, s63, s33
	v_lshl_add_u64 v[148:149], v[148:149], 0, s[66:67]
	s_mov_b32 m0, s36
	ds_read_b128 v[184:187], v154 offset:49152
	ds_read_b128 v[188:191], v154 offset:50176
	ds_read_b128 v[192:195], v154 offset:51200
	ds_read_b128 v[196:199], v154 offset:52224
	ds_read_b128 v[212:215], v154 offset:53248
	ds_read_b128 v[216:219], v154 offset:54272
	ds_read_b128 v[220:223], v154 offset:55296
	ds_read_b128 v[224:227], v154 offset:56320
	global_load_lds_dwordx4 v[148:149], off
	v_lshl_add_u64 v[148:149], v[200:201], 0, s[66:67]
	s_add_i32 m0, s36, 0x2000
	s_add_i32 s36, s68, s33
	global_load_lds_dwordx4 v[148:149], off
	v_lshl_add_u64 v[148:149], v[202:203], 0, s[66:67]
	s_mov_b32 m0, s36
	s_nop 0
	global_load_lds_dwordx4 v[148:149], off
	v_lshl_add_u64 v[148:149], v[204:205], 0, s[66:67]
	s_add_i32 m0, s36, 0x2000
	s_nop 0
	global_load_lds_dwordx4 v[148:149], off
	v_lshl_add_u64 v[148:149], v[208:209], 0, s[66:67]
	s_mov_b32 m0, s50
	s_nop 0
	global_load_lds_dwordx4 v[148:149], off
	v_lshl_add_u64 v[148:149], v[210:211], 0, s[66:67]
	s_mov_b32 m0, s51
	s_nop 0
	global_load_lds_dwordx4 v[148:149], off
	s_waitcnt vmcnt(8)
	s_waitcnt lgkmcnt(0)
	s_barrier
	s_setprio 1
	s_waitcnt lgkmcnt(0)
	v_mfma_f32_16x16x32_bf16 v[64:67], v[144:147], v[184:187], v[64:67]
	s_add_i32 s55, s55, 1
	s_mul_i32 s2, s55, s54
	s_mul_hi_u32 s3, s55, s88
	v_mfma_f32_16x16x32_bf16 v[56:59], v[160:163], v[184:187], v[56:59]
	s_add_i32 s3, s3, s2
	s_mul_i32 s2, s55, s88
	s_add_u32 s12, s2, s90
	v_mfma_f32_16x16x32_bf16 v[48:51], v[144:147], v[192:195], v[48:51]
	s_addc_u32 s13, s3, s42
	v_mov_b64_e32 v[242:243], 0xb00
	v_cmp_lt_i64_e64 s[2:3], s[12:13], v[242:243]
	v_mfma_f32_16x16x32_bf16 v[40:43], v[160:163], v[192:195], v[40:43]
	s_ashr_i32 s8, s12, 31
	s_lshr_b32 s8, s8, 29
	s_add_i32 s8, s12, s8
	v_mfma_f32_16x16x32_bf16 v[32:35], v[144:147], v[212:215], v[32:35]
	s_ashr_i32 s9, s8, 3
	s_and_b32 s8, s8, -8
	s_sub_i32 s8, s12, s8
	v_mfma_f32_16x16x32_bf16 v[24:27], v[160:163], v[212:215], v[24:27]
	s_cmp_lt_i32 s8, 0
	s_movk_i32 s10, 0x161
	s_cselect_b32 s10, s10, 0x160
	v_mfma_f32_16x16x32_bf16 v[16:19], v[144:147], v[220:223], v[16:19]
	s_mul_i32 s8, s8, s10
	s_add_i32 s8, s8, s9
	s_mul_hi_i32 s9, s8, 0x2e8ba2e9
	v_mfma_f32_16x16x32_bf16 v[8:11], v[160:163], v[220:223], v[8:11]
	s_lshr_b32 s10, s9, 31
	s_ashr_i32 s9, s9, 5
	s_add_i32 s9, s9, s10
	v_mfma_f32_16x16x32_bf16 v[64:67], v[156:159], v[188:191], v[64:67]
	s_lshl_b32 s10, s9, 3
	s_sub_i32 s11, 0x80, s10
	s_min_i32 s11, s11, 8
	v_mfma_f32_16x16x32_bf16 v[56:59], v[164:167], v[188:191], v[56:59]
	s_abs_i32 s12, s11
	v_cvt_f32_u32_e32 v241, s12
	s_sub_i32 s14, 0, s12
	v_mfma_f32_16x16x32_bf16 v[48:51], v[156:159], v[196:199], v[48:51]
	s_mulk_i32 s9, 0xb0
	s_sub_i32 s9, s8, s9
	v_rcp_iflag_f32_e32 v241, v241
	v_mfma_f32_16x16x32_bf16 v[40:43], v[164:167], v[196:199], v[40:43]
	s_abs_i32 s8, s9
	s_xor_b32 s13, s9, s11
	s_ashr_i32 s13, s13, 31
	v_mfma_f32_16x16x32_bf16 v[32:35], v[156:159], v[216:219], v[32:35]
	v_mul_f32_e32 v241, 0x4f7ffffe, v241
	v_cvt_u32_f32_e32 v241, v241
	s_mov_b32 s56, s55
	v_mfma_f32_16x16x32_bf16 v[24:27], v[164:167], v[216:219], v[24:27]
	v_readfirstlane_b32 s15, v241
	s_mul_i32 s14, s14, s15
	s_mul_hi_u32 s14, s15, s14
	v_mfma_f32_16x16x32_bf16 v[16:19], v[156:159], v[224:227], v[16:19]
	s_add_i32 s15, s15, s14
	s_mul_hi_u32 s14, s8, s15
	s_mul_i32 s15, s14, s12
	v_mfma_f32_16x16x32_bf16 v[8:11], v[164:167], v[224:227], v[8:11]
	s_sub_i32 s8, s8, s15
	s_add_i32 s36, s14, 1
	s_sub_i32 s15, s8, s12
	s_setprio 0
	s_setprio 1
	v_mfma_f32_16x16x32_bf16 v[60:63], v[168:171], v[184:187], v[60:63]
	s_cmp_ge_u32 s8, s12
	s_cselect_b32 s14, s36, s14
	s_cselect_b32 s8, s15, s8
	v_mfma_f32_16x16x32_bf16 v[52:55], v[176:179], v[184:187], v[52:55]
	s_add_i32 s15, s14, 1
	s_cmp_ge_u32 s8, s12
	s_cselect_b32 s8, s15, s14
	v_mfma_f32_16x16x32_bf16 v[44:47], v[168:171], v[192:195], v[44:47]
	s_xor_b32 s8, s8, s13
	s_sub_i32 s8, s8, s13
	s_mul_i32 s11, s8, s11
	v_mfma_f32_16x16x32_bf16 v[36:39], v[176:179], v[192:195], v[36:39]
	s_sub_i32 s9, s9, s11
	s_add_i32 s10, s10, s9
	s_ashr_i32 s11, s10, 31
	v_mfma_f32_16x16x32_bf16 v[28:31], v[168:171], v[212:215], v[28:31]
	s_lshl_b64 s[12:13], s[10:11], 19
	s_add_u32 s12, s38, s12
	s_addc_u32 s13, s39, s13
	v_mfma_f32_16x16x32_bf16 v[20:23], v[176:179], v[212:215], v[20:23]
	s_and_b64 s[14:15], s[2:3], exec
	s_cselect_b32 s11, s13, s47
	s_cselect_b32 s59, s12, s46
	v_mfma_f32_16x16x32_bf16 v[12:15], v[168:171], v[220:223], v[12:15]
	s_ashr_i32 s9, s8, 31
	s_lshl_b64 s[14:15], s[8:9], 19
	s_add_u32 s14, s40, s14
	v_mfma_f32_16x16x32_bf16 v[4:7], v[176:179], v[220:223], v[4:7]
	s_addc_u32 s15, s41, s15
	s_and_b64 s[36:37], s[2:3], exec
	s_cselect_b32 s9, s15, s53
	v_mfma_f32_16x16x32_bf16 v[60:63], v[172:175], v[188:191], v[60:63]
	s_cselect_b32 s60, s14, s52
	s_add_i32 s62, s62, 2
	s_add_u32 s46, s46, 0x100
	v_mfma_f32_16x16x32_bf16 v[52:55], v[180:183], v[188:191], v[52:55]
	s_addc_u32 s47, s47, 0
	s_add_u32 s52, s52, 0x100
	s_addc_u32 s53, s53, 0
	v_mfma_f32_16x16x32_bf16 v[44:47], v[172:175], v[196:199], v[44:47]
	s_add_u32 s36, s46, 0xfffc0080
	s_addc_u32 s37, s47, -1
	s_add_i32 s63, 0, 0x10000
	v_mfma_f32_16x16x32_bf16 v[36:39], v[180:183], v[196:199], v[36:39]
	s_cmp_eq_u32 s62, 12
	s_cselect_b32 s37, s11, s37
	v_mfma_f32_16x16x32_bf16 v[28:31], v[172:175], v[216:219], v[28:31]
	s_cselect_b32 s36, s59, s36
	v_add_u32_e32 v148, s63, v151
	v_mfma_f32_16x16x32_bf16 v[20:23], v[180:183], v[216:219], v[20:23]
	s_cselect_b32 s73, s9, s53
	s_cselect_b32 s72, s60, s52
	v_mfma_f32_16x16x32_bf16 v[12:15], v[172:175], v[224:227], v[12:15]
	s_add_i32 s68, 0, 0x14000
	s_cmp_gt_u32 s62, 13
	v_mfma_f32_16x16x32_bf16 v[4:7], v[180:183], v[224:227], v[4:7]
	s_setprio 0
	s_barrier
	s_cbranch_scc1 .Lpeel_done_727

; #define PG8_BAR __builtin_amdgcn_s_barrier()
; template <class Epi, class Sched, bool ALIGN_EPI = false, bool SP2 = false>
; __device__ __forceinline__ void gemm_phase(PG8_LAS unsigned char* lds, const Gemm g, const Sched& S, const Epi& E, const int tid) {
;     ...
;         if constexpr (ALIGN_EPI) { if (wr == 0) PG8_BAR; }
;         if constexpr (!Epi::AFTER_DRAIN) { E(acc, cur, wr, wc, fr, fq); S.done(cur); }
.Lpeel_done_727:
	s_mov_b32 s32, 1
	s_and_b64 vcc, exec, s[6:7]
	s_cbranch_vccz .LBB0_730
	s_barrier
